# ssd_out<true> epilogue: fp8 Y tile transposed through the wave's dead x LDS slice, 16 scattered dword stores -> 4 coalesced dwordx4 stores
# speedup vs baseline: 1.0268x; 1.0021x over previous
.LBB0_1267:
	s_or_b64 exec, exec, s[0:1]
	v_lshl_add_u64 v[0:1], s[12:13], 2, v[164:165]
	s_waitcnt lgkmcnt(0)
	s_waitcnt lgkmcnt(0)
	s_barrier
	v_lshrrev_b32_e32 v243, 2, v169
	v_and_b32_e32 v242, 3, v219
	v_or_b32_e32 v244, s28, v243
	v_sub_u32_e32 v243, v243, v166
	v_lshlrev_b32_e32 v242, 4, v242
	v_mul_i32_i24_e32 v243, 0xa0, v243
	v_lshl_add_u32 v244, v244, 12, v242
	v_add_u32_e32 v243, v243, v192
	v_add_u32_e32 v244, s12, v244
	v_add_u32_e32 v243, v243, v242
	v_add_u32_e32 v245, v192, v170
	v_add_u32_e32 v246, v197, v170
	v_add_u32_e32 v247, v209, v170
	v_add_u32_e32 v242, v211, v170
	global_load_dwordx4 v[12:15], v[0:1], off
	global_load_dwordx4 v[8:11], v[0:1], off offset:64
	global_load_dwordx4 v[4:7], v[0:1], off offset:128
	s_nop 0
	global_load_dwordx4 v[0:3], v[0:1], off offset:192
	v_lshl_add_u32 v116, v166, 2, s14
	ds_read2_b32 v[96:97], v116 offset1:16
	ds_read2_b32 v[98:99], v116 offset0:64 offset1:80
	ds_read2_b32 v[100:101], v116 offset0:128 offset1:144
	ds_read2_b32 v[102:103], v116 offset0:192 offset1:208
	v_add_u32_e32 v121, 0x400, v116
	s_waitcnt lgkmcnt(3)
	v_mov_b32_e32 v114, v97
	v_mov_b32_e32 v115, v96
	s_waitcnt lgkmcnt(2)
	v_mov_b32_e32 v96, v99
	v_mov_b32_e32 v97, v98
	s_waitcnt lgkmcnt(1)
	v_mov_b32_e32 v98, v101
	v_mov_b32_e32 v99, v100
	s_waitcnt lgkmcnt(0)
	v_mov_b32_e32 v100, v103
	v_mov_b32_e32 v101, v102
	v_pk_add_f32 v[102:103], v[114:115], 0 op_sel_hi:[1,0]
	ds_read2_b32 v[106:107], v121 offset1:16
	ds_read2_b32 v[108:109], v121 offset0:64 offset1:80
	ds_read2_b32 v[110:111], v121 offset0:128 offset1:144
	ds_read2_b32 v[112:113], v121 offset0:192 offset1:208
	v_pk_add_f32 v[96:97], v[102:103], v[96:97]
	s_waitcnt lgkmcnt(3)
	v_mov_b32_e32 v114, v107
	v_pk_add_f32 v[96:97], v[96:97], v[98:99]
	v_mov_b32_e32 v115, v106
	v_pk_add_f32 v[96:97], v[96:97], v[100:101]
	s_waitcnt lgkmcnt(2)
	v_mov_b32_e32 v106, v109
	v_mov_b32_e32 v107, v108
	v_pk_add_f32 v[96:97], v[96:97], v[114:115]
	s_waitcnt lgkmcnt(1)
	v_mov_b32_e32 v108, v111
	v_mov_b32_e32 v109, v110
	v_pk_add_f32 v[96:97], v[96:97], v[106:107]
	s_mov_b32 s0, 0x358637bd
	s_waitcnt lgkmcnt(0)
	v_mov_b32_e32 v110, v113
	v_mov_b32_e32 v111, v112
	v_pk_add_f32 v[96:97], v[96:97], v[108:109]
	v_mov_b64_e32 v[80:81], s[0:1]
	v_pk_add_f32 v[96:97], v[96:97], v[110:111]
	s_mov_b32 s14, 0x3b000000
	v_or_b32_e32 v78, s12, v170
	v_pk_fma_f32 v[96:97], v[96:97], s[14:15], v[80:81] op_sel_hi:[1,0,0]
	s_mov_b32 s12, 0x800000
	v_mul_f32_e32 v32, 0x4b800000, v97
	v_cmp_gt_f32_e64 s[0:1], s12, v97
	v_mov_b32_e32 v120, v33
	v_mov_b32_e32 v117, v33
	v_cndmask_b32_e64 v32, v97, v32, s[0:1]
	v_rsq_f32_e32 v32, v32
	v_mul_f32_e32 v97, 0x4b800000, v96
	v_mov_b32_e32 v118, v33
	v_mov_b32_e32 v119, v33
	v_mul_f32_e32 v100, 0x45800000, v32
	v_cndmask_b32_e64 v32, v32, v100, s[0:1]
	v_pk_mul_f32 v[72:73], v[72:73], v[32:33] op_sel_hi:[1,0]
	v_cmp_gt_f32_e64 s[0:1], s12, v96
	v_pk_mul_f32 v[66:67], v[66:67], v[32:33] op_sel_hi:[1,0]
	v_pk_mul_f32 v[68:69], v[68:69], v[32:33] op_sel_hi:[1,0]
	v_pk_mul_f32 v[62:63], v[62:63], v[32:33] op_sel_hi:[1,0]
	v_pk_mul_f32 v[64:65], v[64:65], v[32:33] op_sel_hi:[1,0]
	v_pk_mul_f32 v[58:59], v[58:59], v[32:33] op_sel_hi:[1,0]
	v_pk_mul_f32 v[60:61], v[60:61], v[32:33] op_sel_hi:[1,0]
	v_pk_mul_f32 v[56:57], v[56:57], v[32:33] op_sel_hi:[1,0]
	v_cndmask_b32_e64 v32, v96, v97, s[0:1]
	v_rsq_f32_e32 v32, v32
	v_ashrrev_i32_e32 v173, 31, v172
	v_ashrrev_i32_e32 v55, 31, v54
	v_lshlrev_b64 v[104:105], 12, v[172:173]
	v_lshlrev_b64 v[54:55], 12, v[54:55]
	v_ashrrev_i32_e32 v79, 31, v78
	v_lshl_add_u64 v[98:99], s[10:11], 0, v[104:105]
	v_lshl_add_u64 v[98:99], v[98:99], 0, v[78:79]
	v_ashrrev_i32_e32 v77, 31, v76
	v_ashrrev_i32_e32 v75, 31, v74
	s_add_i32 s27, s27, s94
	s_xor_b32 s26, s26, 1
	s_cmpk_lt_i32 s27, 0x400
	s_waitcnt vmcnt(3)
	v_pk_mul_f32 v[66:67], v[12:13], v[66:67]
	s_waitcnt vmcnt(2)
	v_pk_mul_f32 v[62:63], v[8:9], v[62:63]
	s_waitcnt vmcnt(1)
	v_pk_mul_f32 v[58:59], v[4:5], v[58:59]
	s_waitcnt vmcnt(0)
	v_pk_mul_f32 v[72:73], v[0:1], v[72:73]
	v_pk_mul_f32 v[56:57], v[2:3], v[56:57]
	v_cvt_pk_fp8_f32 v120, v72, v73
	v_cvt_pk_fp8_f32 v117, v66, v67
	v_cvt_pk_fp8_f32 v118, v62, v63
	v_cvt_pk_fp8_f32 v119, v58, v59
	v_cvt_pk_fp8_f32 v120, v56, v57 op_sel:[0,0,1]
	v_mul_f32_e32 v56, 0x45800000, v32
	v_cndmask_b32_e64 v32, v32, v56, s[0:1]
	v_pk_mul_f32 v[50:51], v[50:51], v[32:33] op_sel_hi:[1,0]
	v_mov_b32_e32 v56, v33
	v_pk_mul_f32 v[50:51], v[12:13], v[50:51]
	v_pk_mul_f32 v[52:53], v[52:53], v[32:33] op_sel_hi:[1,0]
	v_cvt_pk_fp8_f32 v56, v50, v51
	v_pk_mul_f32 v[52:53], v[14:15], v[52:53]
	v_pk_mul_f32 v[46:47], v[46:47], v[32:33] op_sel_hi:[1,0]
	v_pk_mul_f32 v[42:43], v[42:43], v[32:33] op_sel_hi:[1,0]
	v_cvt_pk_fp8_f32 v56, v52, v53 op_sel:[0,0,1]
	v_pk_mul_f32 v[46:47], v[8:9], v[46:47]
	v_mov_b32_e32 v52, v33
	v_cvt_pk_fp8_f32 v52, v46, v47
	v_pk_mul_f32 v[46:47], v[48:49], v[32:33] op_sel_hi:[1,0]
	v_pk_mul_f32 v[42:43], v[4:5], v[42:43]
	v_pk_mul_f32 v[46:47], v[10:11], v[46:47]
	v_pk_mul_f32 v[68:69], v[14:15], v[68:69]
	v_cvt_pk_fp8_f32 v52, v46, v47 op_sel:[0,0,1]
	v_mov_b32_e32 v46, v33
	v_cvt_pk_fp8_f32 v46, v42, v43
	v_pk_mul_f32 v[42:43], v[44:45], v[32:33] op_sel_hi:[1,0]
	v_pk_mul_f32 v[64:65], v[10:11], v[64:65]
	v_pk_mul_f32 v[42:43], v[6:7], v[42:43]
	v_pk_mul_f32 v[28:29], v[28:29], v[32:33] op_sel_hi:[1,0]
	v_pk_mul_f32 v[60:61], v[6:7], v[60:61]
	v_cvt_pk_fp8_f32 v117, v68, v69 op_sel:[0,0,1]
	v_cvt_pk_fp8_f32 v118, v64, v65 op_sel:[0,0,1]
	v_cvt_pk_fp8_f32 v46, v42, v43 op_sel:[0,0,1]
	v_pk_mul_f32 v[28:29], v[0:1], v[28:29]
	v_mov_b32_e32 v58, v33
	v_cvt_pk_fp8_f32 v119, v60, v61 op_sel:[0,0,1]
	v_cvt_pk_fp8_f32 v58, v28, v29
	v_lshl_add_u64 v[50:51], s[10:11], 0, v[54:55]
	v_lshl_add_u64 v[50:51], v[50:51], 0, v[78:79]
	v_pk_mul_f32 v[28:29], v[30:31], v[32:33] op_sel_hi:[1,0]
	ds_write_b32 v245, v117
	ds_write_b32 v245, v118 offset:16
	ds_write_b32 v245, v119 offset:32
	ds_write_b32 v245, v120 offset:48
	ds_write_b32 v246, v56
	ds_write_b32 v246, v52 offset:16
	ds_write_b32 v246, v46 offset:32
	v_pk_mul_f32 v[28:29], v[2:3], v[28:29]
	s_nop 0
	v_cvt_pk_fp8_f32 v58, v28, v29 op_sel:[0,0,1]
	ds_read2_b32 v[28:29], v116 offset0:32 offset1:48
	ds_read2_b32 v[30:31], v116 offset0:96 offset1:112
	ds_read2_b32 v[42:43], v116 offset0:160 offset1:176
	ds_read2_b32 v[44:45], v116 offset0:224 offset1:240
	ds_read2_b32 v[46:47], v121 offset0:32 offset1:48
	ds_read2_b32 v[48:49], v121 offset0:96 offset1:112
	ds_read2_b32 v[52:53], v121 offset0:160 offset1:176
	ds_read2_b32 v[54:55], v121 offset0:224 offset1:240
	s_waitcnt lgkmcnt(7)
	v_mov_b32_e32 v56, v29
	v_mov_b32_e32 v57, v28
	v_pk_add_f32 v[28:29], v[56:57], 0 op_sel_hi:[1,0]
	s_waitcnt lgkmcnt(6)
	v_mov_b32_e32 v56, v31
	v_mov_b32_e32 v57, v30
	v_pk_add_f32 v[28:29], v[28:29], v[56:57]
	s_waitcnt lgkmcnt(5)
	v_mov_b32_e32 v30, v43
	v_mov_b32_e32 v31, v42
	v_pk_add_f32 v[28:29], v[28:29], v[30:31]
	s_waitcnt lgkmcnt(4)
	v_mov_b32_e32 v30, v45
	v_mov_b32_e32 v31, v44
	v_pk_add_f32 v[28:29], v[28:29], v[30:31]
	s_waitcnt lgkmcnt(3)
	v_mov_b32_e32 v30, v47
	v_mov_b32_e32 v31, v46
	v_pk_add_f32 v[28:29], v[28:29], v[30:31]
	s_waitcnt lgkmcnt(2)
	v_mov_b32_e32 v30, v49
	v_mov_b32_e32 v31, v48
	v_pk_add_f32 v[28:29], v[28:29], v[30:31]
	s_waitcnt lgkmcnt(1)
	v_mov_b32_e32 v30, v53
	v_mov_b32_e32 v31, v52
	v_pk_add_f32 v[28:29], v[28:29], v[30:31]
	s_waitcnt lgkmcnt(0)
	v_mov_b32_e32 v30, v55
	v_mov_b32_e32 v31, v54
	v_pk_add_f32 v[28:29], v[28:29], v[30:31]
	ds_write_b32 v246, v58 offset:48
	v_pk_fma_f32 v[28:29], v[28:29], s[14:15], v[80:81] op_sel_hi:[1,0,0]
	s_nop 0
	v_mul_f32_e32 v30, 0x4b800000, v29
	v_cmp_gt_f32_e64 s[0:1], s12, v29
	s_nop 1
	v_cndmask_b32_e64 v29, v29, v30, s[0:1]
	v_rsq_f32_e32 v29, v29
	v_lshlrev_b64 v[30:31], 12, v[76:77]
	v_lshl_add_u64 v[30:31], s[10:11], 0, v[30:31]
	v_lshl_add_u64 v[30:31], v[30:31], 0, v[78:79]
	v_mul_f32_e32 v32, 0x45800000, v29
	v_cndmask_b32_e64 v32, v29, v32, s[0:1]
	v_pk_mul_f32 v[38:39], v[38:39], v[32:33] op_sel_hi:[1,0]
	v_mov_b32_e32 v29, v33
	v_pk_mul_f32 v[38:39], v[12:13], v[38:39]
	v_pk_mul_f32 v[20:21], v[20:21], v[32:33] op_sel_hi:[1,0]
	v_cvt_pk_fp8_f32 v29, v38, v39
	v_pk_mul_f32 v[38:39], v[40:41], v[32:33] op_sel_hi:[1,0]
	v_pk_mul_f32 v[20:21], v[8:9], v[20:21]
	v_pk_mul_f32 v[38:39], v[14:15], v[38:39]
	v_pk_mul_f32 v[16:17], v[16:17], v[32:33] op_sel_hi:[1,0]
	v_cvt_pk_fp8_f32 v29, v38, v39 op_sel:[0,0,1]
	v_mov_b32_e32 v38, v33
	v_cvt_pk_fp8_f32 v38, v20, v21
	v_pk_mul_f32 v[20:21], v[22:23], v[32:33] op_sel_hi:[1,0]
	v_pk_mul_f32 v[16:17], v[4:5], v[16:17]
	v_pk_mul_f32 v[20:21], v[10:11], v[20:21]
	v_cmp_gt_f32_e64 s[0:1], s12, v28
	v_cvt_pk_fp8_f32 v38, v20, v21 op_sel:[0,0,1]
	v_mov_b32_e32 v20, v33
	v_cvt_pk_fp8_f32 v20, v16, v17
	v_pk_mul_f32 v[16:17], v[24:25], v[32:33] op_sel_hi:[1,0]
	v_mov_b32_e32 v21, v33
	v_pk_mul_f32 v[16:17], v[0:1], v[16:17]
	v_pk_mul_f32 v[18:19], v[18:19], v[32:33] op_sel_hi:[1,0]
	v_cvt_pk_fp8_f32 v21, v16, v17
	v_pk_mul_f32 v[16:17], v[26:27], v[32:33] op_sel_hi:[1,0]
	v_pk_mul_f32 v[18:19], v[6:7], v[18:19]
	v_pk_mul_f32 v[16:17], v[2:3], v[16:17]
	v_cvt_pk_fp8_f32 v20, v18, v19 op_sel:[0,0,1]
	v_cvt_pk_fp8_f32 v21, v16, v17 op_sel:[0,0,1]
	v_mul_f32_e32 v16, 0x4b800000, v28
	v_cndmask_b32_e64 v16, v28, v16, s[0:1]
	v_rsq_f32_e32 v16, v16
	ds_write_b32 v247, v29
	ds_write_b32 v247, v38 offset:16
	ds_write_b32 v247, v20 offset:32
	ds_write_b32 v247, v21 offset:48
	v_lshlrev_b64 v[18:19], 12, v[74:75]
	v_mul_f32_e32 v17, 0x45800000, v16
	v_cndmask_b32_e64 v16, v16, v17, s[0:1]
	v_pk_mul_f32 v[20:21], v[94:95], v[16:17] op_sel_hi:[1,0]
	v_mov_b32_e32 v17, v33
	v_pk_mul_f32 v[12:13], v[12:13], v[20:21]
	s_nop 0
	v_cvt_pk_fp8_f32 v17, v12, v13
	v_lshl_add_u64 v[12:13], s[10:11], 0, v[18:19]
	v_pk_mul_f32 v[18:19], v[90:91], v[16:17] op_sel_hi:[1,0]
	s_nop 0
	v_pk_mul_f32 v[14:15], v[14:15], v[18:19]
	s_nop 0
	v_cvt_pk_fp8_f32 v17, v14, v15 op_sel:[0,0,1]
	s_nop 0
	v_pk_mul_f32 v[14:15], v[92:93], v[16:17] op_sel_hi:[1,0]
	s_nop 0
	v_pk_mul_f32 v[8:9], v[8:9], v[14:15]
	v_mov_b32_e32 v14, v33
	v_cvt_pk_fp8_f32 v14, v8, v9
	v_lshl_add_u64 v[8:9], v[12:13], 0, v[78:79]
	v_pk_mul_f32 v[12:13], v[86:87], v[16:17] op_sel_hi:[1,0]
	s_nop 0
	v_pk_mul_f32 v[10:11], v[10:11], v[12:13]
	v_pk_mul_f32 v[12:13], v[82:83], v[16:17] op_sel_hi:[1,0]
	v_cvt_pk_fp8_f32 v14, v10, v11 op_sel:[0,0,1]
	v_pk_mul_f32 v[10:11], v[88:89], v[16:17] op_sel_hi:[1,0]
	v_pk_mul_f32 v[6:7], v[6:7], v[12:13]
	v_pk_mul_f32 v[4:5], v[4:5], v[10:11]
	v_mov_b32_e32 v10, v33
	v_cvt_pk_fp8_f32 v10, v4, v5
	v_pk_mul_f32 v[4:5], v[84:85], v[16:17] op_sel_hi:[1,0]
	v_cvt_pk_fp8_f32 v10, v6, v7 op_sel:[0,0,1]
	v_pk_mul_f32 v[0:1], v[0:1], v[4:5]
	v_mov_b32_e32 v4, v33
	v_cvt_pk_fp8_f32 v4, v0, v1
	v_pk_mul_f32 v[0:1], v[70:71], v[16:17] op_sel_hi:[1,0]
	s_nop 0
	v_pk_mul_f32 v[0:1], v[2:3], v[0:1]
	s_nop 0
	v_cvt_pk_fp8_f32 v4, v0, v1 op_sel:[0,0,1]
	ds_write_b32 v242, v17
	ds_write_b32 v242, v14 offset:16
	ds_write_b32 v242, v10 offset:32
	ds_write_b32 v242, v4 offset:48
	s_waitcnt lgkmcnt(0)
	ds_read_b128 v[0:3], v243
	ds_read_b128 v[4:7], v243 offset:2560
	ds_read_b128 v[8:11], v243 offset:5120
	ds_read_b128 v[12:15], v243 offset:7680
	s_waitcnt lgkmcnt(3)
	global_store_dwordx4 v244, v[0:3], s[10:11]
	v_add_u32_e32 v244, 0x10000, v244
	s_waitcnt lgkmcnt(2)
	global_store_dwordx4 v244, v[4:7], s[10:11]
	v_add_u32_e32 v244, 0x10000, v244
	s_waitcnt lgkmcnt(1)
	global_store_dwordx4 v244, v[8:11], s[10:11]
	v_add_u32_e32 v244, 0x10000, v244
	s_waitcnt lgkmcnt(0)
	global_store_dwordx4 v244, v[12:15], s[10:11]
	s_nop 1
	s_cbranch_scc0 .LBB0_1276
